# v14 variant: all 15360 prologue-main layer-0 expert-weight copy items run in idle waves 3..7 of the layer-0 router phase
# speedup vs baseline: 1.0073x; 1.0029x over previous
; #define LAS __attribute__((address_space(3)))
; template <class T> __device__ __forceinline__ T* wsp(const Frame& F, size_t off) { return (T*)(F.ws + off); }
;     LAS float* scr = (LAS float*)(F.lds + RING_OFF + F.wave * 16384);
;     const int gw = (ncu ? (int)blockIdx.x - cu0 : F.vcu) * NWAVES + F.wave, NGW = (ncu ? ncu : F.G) * NWAVES;
;     bf16* UP = wsp<bf16>(F, WS_WEUP); bf16* DN = wsp<bf16>(F, WS_WEDN);
;     for (int it = it0 + gw; it < it1; it += NGW) {
;         const int e = it / 384, r = it % 384; const size_t eo = (size_t)(layer * 64 + e) * 1024 * 256;
;         if (r < 128) p0_transpose_item(inp(F, I_WGATE) + eo, 1024, 256, UP + (size_t)e * 512 * 1024, 3, scr, r, F.lane);
;         else if (r < 256) p0_transpose_item(inp(F, I_WUP) + eo, 1024, 256, UP + (size_t)e * 512 * 1024, 4, scr, r - 128, F.lane);
;         else p0_transpose_item(inp(F, I_WDOWN) + eo, 256, 1024, DN + (size_t)e * 1024 * 256, 5, scr, r - 256, F.lane, 16.f);
; __device__ __forceinline__ void p0_prologue(Frame& F) {
;     ...
;     if (P0_PARTS & 4) convert_experts(F, 0, (F.G == 256) ? CVT0_LATE + P0_BAL : 0);
.LBB0_121:
	s_movk_i32 s31, 0x23ff
	s_and_b64 s[0:1], s[40:41], exec
	s_cselect_b32 s0, 0, 0x2400
	s_cselect_b32 s31, 0x5fff, s31
	s_add_i32 s1, s77, s0
	s_cmp_gt_i32 s1, s31
	s_cbranch_scc1 .LBB0_132
	s_add_u32 s14, s38, 0x4800000
	s_addc_u32 s15, s39, 0
	s_add_u32 s16, s38, 0x2800000
	v_readlane_b32 s92, v255, 4
	v_readlane_b32 s6, v255, 2
	v_readlane_b32 s28, v255, 0
	s_addc_u32 s17, s39, 0
	v_and_b32_e32 v1, 28, v45
	s_lshl_b32 s18, s1, 6
	s_lshl_b32 s19, s9, 6
	s_lshl_b32 s20, s1, 5
	s_lshl_b32 s21, s9, 5
	s_lshl_b32 s40, s1, 3
	s_lshl_b32 s41, s9, 3
	s_lshl_b32 s42, s1, 1
	s_lshl_b32 s43, s9, 1
	s_add_i32 s44, 0, 0x202a8
	v_mov_b32_e32 v7, 0
	s_movk_i32 s45, 0x1000
	s_movk_i32 s46, 0x2000
	s_movk_i32 s47, 0x4000
	s_movk_i32 s48, 0x6000
	s_movk_i32 s49, 0x7000
	s_mov_b32 s0, 0x41800000
	s_movk_i32 s50, 0x7fff
	s_mov_b32 s51, 0xffff0000
	s_mov_b64 s[2:3], 0x600
	s_add_i32 s52, 0, 0x202a0
	s_add_i32 s53, 0, 0x20298
	v_mov_b32_e32 v10, 1
	v_mov_b32_e32 v11, 0x400
	v_mov_b32_e32 v12, 0x7c
	v_readlane_b32 s93, v255, 5
	v_readlane_b32 s7, v255, 3
	v_readlane_b32 s29, v255, 1
	s_branch .LBB0_124

; #define LAS __attribute__((address_space(3)))
; template <class T> __device__ __forceinline__ T* wsp(const Frame& F, size_t off) { return (T*)(F.ws + off); }
;     LAS float* scr = (LAS float*)(F.lds + RING_OFF + F.wave * 16384);
;     const int gw = (ncu ? (int)blockIdx.x - cu0 : F.vcu) * NWAVES + F.wave, NGW = (ncu ? ncu : F.G) * NWAVES;
;     bf16* UP = wsp<bf16>(F, WS_WEUP); bf16* DN = wsp<bf16>(F, WS_WEDN);
;     for (int it = it0 + gw; it < it1; it += NGW) {
;         const int e = it / 384, r = it % 384; const size_t eo = (size_t)(layer * 64 + e) * 1024 * 256;
;         if (r < 128) p0_transpose_item(inp(F, I_WGATE) + eo, 1024, 256, UP + (size_t)e * 512 * 1024, 3, scr, r, F.lane);
;         else if (r < 256) p0_transpose_item(inp(F, I_WUP) + eo, 1024, 256, UP + (size_t)e * 512 * 1024, 4, scr, r - 128, F.lane);
;         else p0_transpose_item(inp(F, I_WDOWN) + eo, 256, 1024, DN + (size_t)e * 1024 * 256, 5, scr, r - 256, F.lane, 16.f);
.Lcv0_entry:
	s_cmpk_lg_i32 s67, 0x100
	s_cbranch_scc1 .Lcv0_end
	v_mov_b32_e32 v2, v0
	s_mul_i32 s4, s71, 5
	s_movk_i32 s2, 0x500
	v_readfirstlane_b32 s5, v2
	s_movk_i32 s3, 0x2000
	s_ashr_i32 s5, s5, 6
	s_cmpk_lt_i32 s5, 3
	s_cbranch_scc1 .Lcv0_end
	s_add_i32 s5, s5, s4
	s_addk_i32 s5, 0x23fd
	s_cmpk_gt_i32 s5, 0x5fff
	s_cbranch_scc1 .Lcv0_end
	s_add_u32 s9, s38, 0x4800000
	s_addc_u32 s18, s39, 0
	s_add_u32 s19, s38, 0x2800000
	v_and_b32_e32 v1, 56, v2
	v_lshlrev_b32_e32 v2, 2, v2
	s_addc_u32 s20, s39, 0
	v_and_b32_e32 v10, 28, v2
	s_lshl_b32 s21, s5, 6
	s_lshl_b32 s22, s2, 6
	s_lshl_b32 s23, s5, 5
	s_lshl_b32 s40, s2, 5
	s_lshl_b32 s41, s5, 3
	s_lshl_b32 s42, s2, 3
	s_lshl_b32 s43, s5, 1
	s_lshl_b32 s44, s2, 1
	s_add_i32 s45, 0, 0x202a8
	s_waitcnt lgkmcnt(1)
	v_mov_b32_e32 v7, 0
	s_movk_i32 s46, 0x1000
	s_movk_i32 s47, 0x4000
	s_movk_i32 s48, 0x6000
	s_movk_i32 s49, 0x7000
	s_mov_b32 s4, 0x41800000
	s_movk_i32 s50, 0x7fff
	s_mov_b32 s51, 0xffff0000
	s_mov_b64 s[10:11], 0x600
	s_add_i32 s52, 0, 0x202a0
	s_add_i32 s53, 0, 0x20298
	v_mov_b32_e32 v11, 1
	v_mov_b32_e32 v12, 0x400
	v_mov_b32_e32 v13, 0x7c
	s_branch .Lcv0_07
